# best9 + LN3 router: slot atomics software-pipelined (token table stores deferred one row so the atomic round trip overlaps the next row's LN)
# baseline (speedup 1.0000x reference)
.LBB0_1874:
	s_mov_b32 s98, 0
	s_cmp_lt_i32 s76, 17
	s_cselect_b64 s[0:1], -1, 0
	s_and_b64 s[22:23], s[0:1], s[4:5]
	s_andn2_b64 vcc, exec, s[22:23]
	s_cbranch_vccnz .LBB0_1889
	v_or_b32_e32 v1, 0x200, v0
	s_waitcnt vmcnt(0)
	v_mov_b32_e32 v6, 16
	s_mov_b64 s[0:1], 0
	v_mov_b32_e32 v5, 0
	v_mov_b64_e32 v[2:3], v[0:1]
	s_waitcnt lgkmcnt(0)
	s_barrier

.LBB0_1886:
	s_waitcnt vmcnt(3)
	v_cvt_f32_f16_e32 v20, v2
	s_waitcnt lgkmcnt(1)
	v_cvt_f32_f16_sdwa v21, v2 dst_sel:DWORD dst_unused:UNUSED_PAD src0_sel:WORD_1
	v_cvt_f32_f16_e32 v2, v3
	v_cvt_f32_f16_sdwa v3, v3 dst_sel:DWORD dst_unused:UNUSED_PAD src0_sel:WORD_1
	v_cvt_f32_f16_sdwa v19, v5 dst_sel:DWORD dst_unused:UNUSED_PAD src0_sel:WORD_1
	v_cvt_f32_f16_e32 v18, v5
	v_cvt_f32_f16_sdwa v5, v4 dst_sel:DWORD dst_unused:UNUSED_PAD src0_sel:WORD_1
	v_cvt_f32_f16_e32 v4, v4
	v_add_f32_e32 v22, 0, v20
	v_add_f32_e32 v22, v22, v21
	v_add_f32_e32 v22, v22, v2
	v_add_f32_e32 v22, v22, v3
	v_add_f32_e32 v22, v22, v4
	s_waitcnt vmcnt(2)
	v_cvt_f32_f16_e32 v26, v6
	v_add_f32_e32 v22, v22, v5
	v_cvt_f32_f16_sdwa v27, v6 dst_sel:DWORD dst_unused:UNUSED_PAD src0_sel:WORD_1
	v_add_f32_e32 v22, v22, v18
	v_cvt_f32_f16_e32 v6, v7
	v_add_f32_e32 v28, v22, v19
	v_cvt_f32_f16_sdwa v7, v7 dst_sel:DWORD dst_unused:UNUSED_PAD src0_sel:WORD_1
	s_waitcnt vmcnt(0) lgkmcnt(0)
	v_cvt_f32_f16_sdwa v23, v17 dst_sel:DWORD dst_unused:UNUSED_PAD src0_sel:WORD_1
	v_cvt_f32_f16_e32 v22, v17
	v_cvt_f32_f16_sdwa v25, v9 dst_sel:DWORD dst_unused:UNUSED_PAD src0_sel:WORD_1
	v_cvt_f32_f16_e32 v24, v9
	v_cvt_f32_f16_sdwa v9, v8 dst_sel:DWORD dst_unused:UNUSED_PAD src0_sel:WORD_1
	v_cvt_f32_f16_e32 v8, v8
	v_add_f32_e32 v17, v28, v26
	v_add_f32_e32 v17, v17, v27
	v_add_f32_e32 v17, v17, v6
	v_add_f32_e32 v17, v17, v7
	v_add_f32_e32 v17, v17, v8
	v_cvt_f32_f16_e32 v30, v10
	v_add_f32_e32 v17, v17, v9
	v_cvt_f32_f16_sdwa v31, v10 dst_sel:DWORD dst_unused:UNUSED_PAD src0_sel:WORD_1
	v_add_f32_e32 v17, v17, v24
	v_cvt_f32_f16_e32 v10, v11
	v_add_f32_e32 v17, v17, v25
	v_cvt_f32_f16_sdwa v11, v11 dst_sel:DWORD dst_unused:UNUSED_PAD src0_sel:WORD_1
	v_cvt_f32_f16_sdwa v29, v13 dst_sel:DWORD dst_unused:UNUSED_PAD src0_sel:WORD_1
	v_cvt_f32_f16_e32 v28, v13
	v_cvt_f32_f16_sdwa v13, v12 dst_sel:DWORD dst_unused:UNUSED_PAD src0_sel:WORD_1
	v_cvt_f32_f16_e32 v12, v12
	v_add_f32_e32 v17, v17, v30
	v_add_f32_e32 v17, v17, v31
	v_add_f32_e32 v17, v17, v10
	v_add_f32_e32 v17, v17, v11
	v_add_f32_e32 v17, v17, v12
	v_cvt_f32_f16_e32 v32, v14
	v_add_f32_e32 v17, v17, v13
	v_cvt_f32_f16_sdwa v74, v14 dst_sel:DWORD dst_unused:UNUSED_PAD src0_sel:WORD_1
	v_cvt_f32_f16_e32 v38, v15
	v_add_f32_e32 v17, v17, v28
	v_cvt_f32_f16_sdwa v58, v15 dst_sel:DWORD dst_unused:UNUSED_PAD src0_sel:WORD_1
	v_add_f32_e32 v17, v17, v29
	v_cvt_f32_f16_e32 v33, v16
	v_add_f32_e32 v14, v17, v32
	v_cvt_f32_f16_sdwa v75, v16 dst_sel:DWORD dst_unused:UNUSED_PAD src0_sel:WORD_1
	v_add_f32_e32 v14, v14, v74
	v_add_f32_e32 v14, v14, v38
	v_add_f32_e32 v14, v14, v58
	v_add_f32_e32 v14, v14, v33
	v_add_f32_e32 v14, v14, v75
	v_add_f32_e32 v14, v14, v22
	v_add_f32_e32 v14, v14, v23
	ds_bpermute_b32 v16, v1, v14
	global_load_dwordx4 v[58:61], v[42:43], off offset:16
	global_load_dwordx4 v[62:65], v[42:43], off
	global_load_dwordx4 v[66:69], v[44:45], off offset:16
	global_load_dwordx4 v[70:73], v[44:45], off
	global_load_dwordx4 v[100:103], v[42:43], off offset:2064
	global_load_dwordx4 v[104:107], v[42:43], off offset:2048
	global_load_dwordx4 v[108:111], v[44:45], off offset:2048
	global_load_dwordx4 v[112:115], v[44:45], off offset:2064
	global_load_dwordx4 v[116:119], v[46:47], off offset:16
	global_load_dwordx4 v[120:123], v[46:47], off
	global_load_dwordx4 v[124:127], v[48:49], off
	global_load_dwordx4 v[128:131], v[48:49], off offset:16
	s_waitcnt lgkmcnt(0)
	v_add_f32_e32 v14, v14, v16
	ds_bpermute_b32 v16, v88, v14
	v_add_u32_e32 v99, s26, v34
	v_cmp_gt_i32_e32 vcc, s3, v99
	v_cmp_lt_i32_e64 s[6:7], s27, v99
	s_waitcnt lgkmcnt(0)
	v_add_f32_e32 v14, v14, v16
	ds_bpermute_b32 v16, v89, v14
	s_waitcnt lgkmcnt(0)
	v_add_f32_e32 v14, v14, v16
	ds_bpermute_b32 v16, v90, v14
	s_waitcnt lgkmcnt(0)
	v_add_f32_e32 v14, v14, v16
	ds_bpermute_b32 v16, v91, v14
	s_waitcnt lgkmcnt(0)
	v_add_f32_e32 v14, v14, v16
	ds_bpermute_b32 v16, v92, v14
	s_waitcnt lgkmcnt(0)
	v_add_f32_e32 v38, v14, v16
	v_mul_f32_e32 v14, 0x3a000000, v38
	v_pk_add_f32 v[76:77], v[20:21], v[14:15] op_sel_hi:[1,0] neg_lo:[0,1] neg_hi:[0,1]
	v_pk_add_f32 v[78:79], v[2:3], v[14:15] op_sel_hi:[1,0] neg_lo:[0,1] neg_hi:[0,1]
	v_pk_mul_f32 v[16:17], v[76:77], v[76:77]
	v_pk_mul_f32 v[2:3], v[78:79], v[78:79]
	v_add_f32_e32 v16, v16, v17
	v_pk_add_f32 v[82:83], v[4:5], v[14:15] op_sel_hi:[1,0] neg_lo:[0,1] neg_hi:[0,1]
	v_add_f32_e32 v2, v2, v16
	v_pk_mul_f32 v[4:5], v[82:83], v[82:83]
	v_add_f32_e32 v2, v3, v2
	v_pk_add_f32 v[132:133], v[18:19], v[14:15] op_sel_hi:[1,0] neg_lo:[0,1] neg_hi:[0,1]
	v_add_f32_e32 v2, v4, v2
	v_pk_mul_f32 v[18:19], v[132:133], v[132:133]
	v_add_f32_e32 v2, v5, v2
	v_pk_add_f32 v[134:135], v[26:27], v[14:15] op_sel_hi:[1,0] neg_lo:[0,1] neg_hi:[0,1]
	v_add_f32_e32 v2, v18, v2
	v_pk_mul_f32 v[20:21], v[134:135], v[134:135]
	v_add_f32_e32 v2, v19, v2
	v_pk_add_f32 v[136:137], v[6:7], v[14:15] op_sel_hi:[1,0] neg_lo:[0,1] neg_hi:[0,1]
	v_add_f32_e32 v2, v20, v2
	v_pk_mul_f32 v[6:7], v[136:137], v[136:137]
	v_add_f32_e32 v2, v21, v2
	v_pk_add_f32 v[138:139], v[8:9], v[14:15] op_sel_hi:[1,0] neg_lo:[0,1] neg_hi:[0,1]
	v_add_f32_e32 v2, v6, v2
	v_pk_mul_f32 v[8:9], v[138:139], v[138:139]
	v_add_f32_e32 v2, v7, v2
	v_pk_add_f32 v[140:141], v[24:25], v[14:15] op_sel_hi:[1,0] neg_lo:[0,1] neg_hi:[0,1]
	v_add_f32_e32 v2, v8, v2
	v_pk_mul_f32 v[24:25], v[140:141], v[140:141]
	v_add_f32_e32 v2, v9, v2
	v_pk_add_f32 v[142:143], v[30:31], v[14:15] op_sel_hi:[1,0] neg_lo:[0,1] neg_hi:[0,1]
	v_add_f32_e32 v2, v24, v2
	v_pk_mul_f32 v[26:27], v[142:143], v[142:143]
	v_add_f32_e32 v2, v25, v2
	v_pk_add_f32 v[144:145], v[10:11], v[14:15] op_sel_hi:[1,0] neg_lo:[0,1] neg_hi:[0,1]
	v_add_f32_e32 v2, v26, v2
	v_pk_mul_f32 v[10:11], v[144:145], v[144:145]
	v_add_f32_e32 v2, v27, v2
	v_pk_add_f32 v[146:147], v[12:13], v[14:15] op_sel_hi:[1,0] neg_lo:[0,1] neg_hi:[0,1]
	v_add_f32_e32 v2, v10, v2
	v_pk_mul_f32 v[12:13], v[146:147], v[146:147]
	v_add_f32_e32 v2, v11, v2
	v_pk_add_f32 v[148:149], v[28:29], v[14:15] op_sel_hi:[1,0] neg_lo:[0,1] neg_hi:[0,1]
	v_add_f32_e32 v2, v12, v2
	v_pk_mul_f32 v[28:29], v[148:149], v[148:149]
	v_add_f32_e32 v2, v13, v2
	v_pk_add_f32 v[150:151], v[32:33], v[14:15] op_sel_hi:[1,0] neg_lo:[0,1] neg_hi:[0,1]
	v_add_f32_e32 v2, v28, v2
	v_pk_mul_f32 v[30:31], v[150:151], v[150:151]
	v_pk_add_f32 v[152:153], v[74:75], v[14:15] op_sel_hi:[1,0] neg_lo:[0,1] neg_hi:[0,1]
	v_add_f32_e32 v2, v29, v2
	v_pk_mul_f32 v[32:33], v[152:153], v[152:153]
	v_add_f32_e32 v2, v30, v2
	v_add_f32_e32 v2, v32, v2
	v_fma_mix_f32 v154, v38, s33, v15 op_sel_hi:[0,0,1]
	v_fmac_f32_e32 v2, v154, v154
	v_fma_mix_f32 v84, v38, s33, v15 op_sel:[0,0,1] op_sel_hi:[0,0,1]
	v_fmac_f32_e32 v2, v84, v84
	v_add_f32_e32 v2, v31, v2
	v_add_f32_e32 v4, v33, v2
	v_pk_add_f32 v[86:87], v[22:23], v[14:15] op_sel_hi:[1,0] neg_lo:[0,1] neg_hi:[0,1]
	global_load_dwordx4 v[30:33], v[50:51], off
	global_load_dwordx4 v[18:21], v[50:51], off offset:16
	global_load_dwordx4 v[26:29], v[52:53], off
	global_load_dwordx4 v[22:25], v[52:53], off offset:16
	v_pk_mul_f32 v[2:3], v[86:87], v[86:87]
	v_mov_b32_e32 v155, v86
	v_add_f32_e32 v2, v2, v4
	v_add_f32_e32 v2, v3, v2
	ds_bpermute_b32 v3, v1, v2
	s_waitcnt lgkmcnt(0)
	v_add_f32_e32 v2, v2, v3
	ds_bpermute_b32 v3, v88, v2
	s_waitcnt lgkmcnt(0)
	v_add_f32_e32 v2, v2, v3
	ds_bpermute_b32 v3, v89, v2
	s_waitcnt lgkmcnt(0)
	v_add_f32_e32 v2, v2, v3
	ds_bpermute_b32 v3, v90, v2
	s_waitcnt lgkmcnt(0)
	v_add_f32_e32 v2, v2, v3
	ds_bpermute_b32 v3, v91, v2
	s_waitcnt lgkmcnt(0)
	v_add_f32_e32 v3, v2, v3
	ds_bpermute_b32 v4, v92, v3
	v_cndmask_b32_e32 v2, v34, v99, vcc
	s_waitcnt lgkmcnt(0)
	v_add_f32_e32 v3, v3, v4
	v_fmamk_f32 v3, v3, 0x3a000000, v35
	v_mul_f32_e32 v4, 0x4f800000, v3
	v_cmp_gt_f32_e32 vcc, s44, v3
	s_nop 1
	v_cndmask_b32_e32 v4, v3, v4, vcc
	v_sqrt_f32_e32 v5, v4
	v_ashrrev_i32_e32 v3, 31, v2
	v_lshlrev_b64 v[2:3], 12, v[2:3]
	v_lshl_add_u64 v[14:15], v[40:41], 0, v[2:3]
	v_add_u32_e32 v2, -1, v5
	v_fma_f32 v3, -v2, v5, v4
	v_cmp_ge_f32_e64 s[0:1], 0, v3
	v_add_u32_e32 v3, 1, v5
	s_nop 0
	v_cndmask_b32_e64 v2, v5, v2, s[0:1]
	v_fma_f32 v5, -v3, v5, v4
	v_cmp_lt_f32_e64 s[0:1], 0, v5
	s_nop 1
	v_cndmask_b32_e64 v2, v2, v3, s[0:1]
	v_mul_f32_e32 v3, 0x37800000, v2
	v_cndmask_b32_e32 v2, v2, v3, vcc
	v_cmp_class_f32_e32 vcc, v4, v94
	s_nop 1
	v_cndmask_b32_e32 v38, v2, v4, vcc
	v_div_scale_f32 v74, s[0:1], v38, v38, 1.0
	v_rcp_f32_e32 v75, v74
	global_load_dwordx4 v[2:5], v[14:15], off
	global_load_dwordx4 v[6:9], v[14:15], off offset:1024
	global_load_dwordx4 v[10:13], v[14:15], off offset:2048
	s_nop 0
	global_load_dwordx4 v[14:17], v[14:15], off offset:3072
	v_fma_f32 v80, -v74, v75, 1.0
	v_fmac_f32_e32 v75, v80, v75
	v_div_scale_f32 v80, vcc, 1.0, v38, 1.0
	v_mul_f32_e32 v81, v80, v75
	v_fma_f32 v85, -v74, v81, v80
	v_fmac_f32_e32 v81, v85, v75
	v_fma_f32 v74, -v74, v81, v80
	v_div_fmas_f32 v74, v74, v75, v81
	v_div_fixup_f32 v38, v74, v38, 1.0
	v_pk_mul_f32 v[74:75], v[76:77], v[38:39] op_sel_hi:[1,0]
	s_waitcnt vmcnt(16)
	v_pk_fma_f32 v[80:81], v[62:63], v[74:75], v[70:71]
	v_pk_mul_f32 v[62:63], v[82:83], v[38:39] op_sel_hi:[1,0]
	s_nop 0
	v_pk_fma_f32 v[82:83], v[58:59], v[62:63], v[66:67]
	v_pk_mul_f32 v[58:59], v[78:79], v[38:39] op_sel_hi:[1,0]
	v_pk_mul_f32 v[62:63], v[150:151], v[38:39] op_sel_hi:[1,0]
	v_pk_fma_f32 v[74:75], v[64:65], v[58:59], v[72:73]
	v_pk_mul_f32 v[58:59], v[132:133], v[38:39] op_sel_hi:[1,0]
	v_mul_f32_e32 v85, 0x41800000, v74
	v_pk_fma_f32 v[78:79], v[60:61], v[58:59], v[68:69]
	v_pk_mul_f32 v[58:59], v[134:135], v[38:39] op_sel_hi:[1,0]
	v_pk_mul_f32 v[60:61], v[148:149], v[38:39] op_sel_hi:[1,0]
	s_waitcnt vmcnt(13)
	v_pk_fma_f32 v[72:73], v[104:105], v[58:59], v[108:109]
	v_pk_mul_f32 v[58:59], v[138:139], v[38:39] op_sel_hi:[1,0]
	v_lshl_add_u64 v[104:105], s[58:59], 0, v[36:37]
	s_waitcnt vmcnt(12)
	v_pk_fma_f32 v[76:77], v[100:101], v[58:59], v[112:113]
	v_pk_mul_f32 v[58:59], v[136:137], v[38:39] op_sel_hi:[1,0]
	s_waitcnt vmcnt(7)
	v_mov_b32_e32 v100, v30
	v_pk_fma_f32 v[66:67], v[106:107], v[58:59], v[110:111]
	v_pk_mul_f32 v[58:59], v[140:141], v[38:39] op_sel_hi:[1,0]
	s_waitcnt vmcnt(6)
	v_mov_b32_e32 v101, v18
	v_pk_fma_f32 v[70:71], v[102:103], v[58:59], v[114:115]
	s_waitcnt vmcnt(4)
	v_mov_b32_e32 v103, v22
	v_cvt_pk_f16_f32 v22, v80, v81
	v_mov_b32_e32 v102, v26
	v_add_u32_e32 v22, 0x20002, v22
	v_pk_fma_f32 v[62:63], v[100:101], v[62:63], v[102:103]
	v_and_b32_e32 v100, 0xfffcfffc, v22
	v_cvt_pk_f16_f32 v22, v74, v75
	v_add_u32_e32 v22, 0x20002, v22
	v_and_b32_e32 v101, 0xfffcfffc, v22
	v_cvt_pk_f16_f32 v22, v82, v83
	v_add_u32_e32 v22, 0x20002, v22
	v_and_b32_e32 v102, 0xfffcfffc, v22
	v_cvt_pk_f16_f32 v22, v78, v79
	v_add_u32_e32 v22, 0x20002, v22
	v_and_b32_e32 v103, 0xfffcfffc, v22
	v_add_co_u32_e32 v134, vcc, s45, v104
	v_cvt_pk_f16_f32 v22, v72, v73
	s_nop 0
	v_addc_co_u32_e32 v135, vcc, 0, v105, vcc
	v_add_u32_e32 v22, 0x20002, v22
	global_store_dwordx4 v[134:135], v[100:103], off
	v_pk_mul_f32 v[58:59], v[142:143], v[38:39] op_sel_hi:[1,0]
	v_pk_fma_f32 v[60:61], v[118:119], v[60:61], v[130:131]
	v_and_b32_e32 v100, 0xfffcfffc, v22
	v_cvt_pk_f16_f32 v22, v66, v67
	v_add_u32_e32 v22, 0x20002, v22
	v_and_b32_e32 v101, 0xfffcfffc, v22
	v_cvt_pk_f16_f32 v22, v76, v77
	v_add_u32_e32 v22, 0x20002, v22
	v_and_b32_e32 v102, 0xfffcfffc, v22
	v_cvt_pk_f16_f32 v22, v70, v71
	v_pk_fma_f32 v[64:65], v[120:121], v[58:59], v[124:125]
	v_pk_mul_f32 v[58:59], v[146:147], v[38:39] op_sel_hi:[1,0]
	v_add_u32_e32 v22, 0x20002, v22
	v_pk_fma_f32 v[68:69], v[116:117], v[58:59], v[128:129]
	v_pk_mul_f32 v[58:59], v[144:145], v[38:39] op_sel_hi:[1,0]
	v_and_b32_e32 v103, 0xfffcfffc, v22
	v_cvt_pk_f16_f32 v22, v64, v65
	v_pk_fma_f32 v[58:59], v[122:123], v[58:59], v[126:127]
	v_add_u32_e32 v22, 0x20002, v22
	global_store_dwordx4 v[134:135], v[100:103], off offset:1024
	v_mul_f32_e32 v26, 0x41800000, v81
	v_med3_f32 v26, v26, s46, v96
	v_and_b32_e32 v100, 0xfffcfffc, v22
	v_cvt_pk_f16_f32 v22, v58, v59
	v_add_u32_e32 v22, 0x20002, v22
	v_and_b32_e32 v101, 0xfffcfffc, v22
	v_cvt_pk_f16_f32 v22, v68, v69
	v_add_u32_e32 v22, 0x20002, v22
	v_and_b32_e32 v102, 0xfffcfffc, v22
	v_cvt_pk_f16_f32 v22, v60, v61
	v_add_u32_e32 v22, 0x20002, v22
	v_and_b32_e32 v103, 0xfffcfffc, v22
	v_mul_f32_e32 v22, 0x41800000, v80
	v_med3_f32 v22, v22, s46, v96
	v_mov_b32_e32 v136, 0
	v_cvt_pk_fp8_f32 v136, v22, v26
	v_mul_f32_e32 v22, 0x41800000, v75
	v_med3_f32 v26, v85, s46, v96
	v_med3_f32 v22, v22, s46, v96
	v_cvt_pk_fp8_f32 v136, v26, v22 op_sel:[0,0,1]
	v_mul_f32_e32 v22, 0x41800000, v82
	v_mul_f32_e32 v26, 0x41800000, v83
	v_med3_f32 v22, v22, s46, v96
	v_med3_f32 v26, v26, s46, v96
	v_mov_b32_e32 v137, 0
	v_cvt_pk_fp8_f32 v137, v22, v26
	v_mul_f32_e32 v85, 0x41800000, v78
	v_mul_f32_e32 v22, 0x41800000, v79
	v_med3_f32 v26, v85, s46, v96
	v_med3_f32 v22, v22, s46, v96
	v_cvt_pk_fp8_f32 v137, v26, v22 op_sel:[0,0,1]
	v_mul_f32_e32 v22, 0x41800000, v72
	v_mul_f32_e32 v26, 0x41800000, v73
	v_med3_f32 v22, v22, s46, v96
	v_med3_f32 v26, v26, s46, v96
	v_mov_b32_e32 v140, 0
	v_cvt_pk_fp8_f32 v140, v22, v26
	v_mul_f32_e32 v85, 0x41800000, v66
	v_mul_f32_e32 v22, 0x41800000, v67
	v_med3_f32 v26, v85, s46, v96
	v_med3_f32 v22, v22, s46, v96
	v_cvt_pk_fp8_f32 v140, v26, v22 op_sel:[0,0,1]
	v_mul_f32_e32 v22, 0x41800000, v76
	v_mul_f32_e32 v26, 0x41800000, v77
	v_med3_f32 v22, v22, s46, v96
	v_med3_f32 v26, v26, s46, v96
	v_mov_b32_e32 v141, 0
	v_cvt_pk_fp8_f32 v141, v22, v26
	v_mul_f32_e32 v85, 0x41800000, v70
	v_mul_f32_e32 v22, 0x41800000, v71
	v_med3_f32 v26, v85, s46, v96
	v_med3_f32 v22, v22, s46, v96
	v_cvt_pk_fp8_f32 v141, v26, v22 op_sel:[0,0,1]
	v_mul_f32_e32 v22, 0x41800000, v64
	v_mul_f32_e32 v26, 0x41800000, v65
	v_med3_f32 v22, v22, s46, v96
	v_med3_f32 v26, v26, s46, v96
	v_mov_b32_e32 v142, 0
	v_cvt_pk_fp8_f32 v142, v22, v26
	v_mul_f32_e32 v85, 0x41800000, v58
	v_mul_f32_e32 v22, 0x41800000, v59
	v_med3_f32 v26, v85, s46, v96
	v_med3_f32 v22, v22, s46, v96
	v_cvt_pk_fp8_f32 v142, v26, v22 op_sel:[0,0,1]
	v_mul_f32_e32 v22, 0x41800000, v68
	v_mul_f32_e32 v26, 0x41800000, v69
	v_med3_f32 v22, v22, s46, v96
	v_med3_f32 v26, v26, s46, v96
	v_mov_b32_e32 v143, 0
	v_cvt_pk_fp8_f32 v143, v22, v26
	v_mul_f32_e32 v85, 0x41800000, v60
	v_mul_f32_e32 v22, 0x41800000, v61
	v_med3_f32 v26, v85, s46, v96
	v_med3_f32 v22, v22, s46, v96
	v_cvt_pk_fp8_f32 v143, v26, v22 op_sel:[0,0,1]
	v_mul_f32_e32 v22, 0x41800000, v62
	v_med3_f32 v86, v22, s46, v96
	v_mul_f32_e32 v22, 0x41800000, v63
	v_pk_mul_f32 v[132:133], v[152:153], v[38:39] op_sel_hi:[1,0]
	v_mov_b32_e32 v18, v31
	v_med3_f32 v144, v22, s46, v96
	v_mov_b32_e32 v22, v27
	v_pk_mul_f32 v[30:31], v[154:155], v[38:39] op_sel_hi:[1,0]
	v_pk_fma_f32 v[18:19], v[18:19], v[132:133], v[22:23]
	v_mov_b32_e32 v22, v32
	v_mov_b32_e32 v23, v20
	v_mov_b32_e32 v26, v28
	v_mov_b32_e32 v27, v24
	v_mov_b32_e32 v85, v87
	v_pk_fma_f32 v[22:23], v[22:23], v[30:31], v[26:27]
	v_pk_mul_f32 v[26:27], v[84:85], v[38:39] op_sel_hi:[1,0]
	v_mov_b32_e32 v20, v33
	v_mov_b32_e32 v24, v29
	v_pk_fma_f32 v[20:21], v[20:21], v[26:27], v[24:25]
	v_cvt_pk_f16_f32 v24, v62, v18
	v_cvt_pk_f16_f32 v25, v22, v20
	v_cvt_pk_f16_f32 v26, v63, v19
	v_cvt_pk_f16_f32 v27, v23, v21
	v_add_u32_e32 v24, 0x20002, v24
	v_add_u32_e32 v25, 0x20002, v25
	v_add_u32_e32 v26, 0x20002, v26
	v_add_u32_e32 v27, 0x20002, v27
	global_store_dwordx4 v[134:135], v[100:103], off offset:2048
	v_and_b32_e32 v24, 0xfffcfffc, v24
	v_and_b32_e32 v25, 0xfffcfffc, v25
	v_and_b32_e32 v26, 0xfffcfffc, v26
	v_and_b32_e32 v27, 0xfffcfffc, v27
	ds_read_b128 v[100:103], v93
	ds_read_b128 v[104:107], v93 offset:16
	ds_read_b128 v[108:111], v93 offset:2048
	ds_read_b128 v[112:115], v93 offset:2064
	ds_read_b128 v[116:119], v93 offset:4096
	ds_read_b128 v[120:123], v93 offset:4112
	ds_read_b128 v[124:127], v93 offset:6144
	ds_read_b128 v[128:131], v93 offset:6160
	global_store_dwordx4 v[134:135], v[24:27], off offset:3072
	v_lshl_add_u64 v[138:139], s[58:59], 0, v[56:57]
	s_waitcnt lgkmcnt(6)
	v_mov_b32_e32 v84, v104
	v_mul_f32_e32 v26, 0x41800000, v18
	v_med3_f32 v28, v26, s46, v96
	v_mov_b32_e32 v26, 0
	v_cvt_pk_fp8_f32 v26, v86, v28
	v_mul_f32_e32 v27, 0x41800000, v22
	v_mul_f32_e32 v28, 0x41800000, v20
	v_med3_f32 v27, v27, s46, v96
	v_med3_f32 v28, v28, s46, v96
	v_cvt_pk_fp8_f32 v26, v27, v28 op_sel:[0,0,1]
	v_mul_f32_e32 v27, 0x41800000, v19
	v_med3_f32 v29, v27, s46, v96
	v_mov_b32_e32 v27, 0
	v_cvt_pk_fp8_f32 v27, v144, v29
	v_mul_f32_e32 v28, 0x41800000, v23
	v_mul_f32_e32 v29, 0x41800000, v21
	v_add_co_u32_e32 v24, vcc, s47, v138
	v_med3_f32 v28, v28, s46, v96
	v_med3_f32 v29, v29, s46, v96
	v_addc_co_u32_e32 v25, vcc, 0, v139, vcc
	v_cvt_pk_fp8_f32 v27, v28, v29 op_sel:[0,0,1]
	global_store_dwordx2 v[24:25], v[136:137], off
	global_store_dwordx2 v[24:25], v[140:141], off offset:512
	global_store_dwordx2 v[24:25], v[142:143], off offset:1024
	global_store_dwordx2 v[24:25], v[26:27], off offset:1536
	ds_read_b128 v[24:27], v93 offset:8192
	ds_read_b128 v[28:31], v93 offset:8208
	v_mov_b32_e32 v32, v100
	s_waitcnt lgkmcnt(1)
	v_mov_b32_e32 v33, v24
	s_waitcnt lgkmcnt(0)
	v_mov_b32_e32 v85, v28
	v_pk_mul_f32 v[144:145], v[84:85], v[82:83] op_sel_hi:[1,0]
	v_mov_b32_e32 v28, v105
	v_pk_fma_f32 v[32:33], v[32:33], v[80:81], v[144:145] op_sel_hi:[1,0,1]
	v_mov_b32_e32 v24, v101
	v_pk_mul_f32 v[28:29], v[28:29], v[82:83] op_sel:[0,1]
	v_pk_add_f32 v[32:33], v[32:33], 0 op_sel_hi:[1,0]
	v_pk_fma_f32 v[24:25], v[24:25], v[80:81], v[28:29] op_sel:[0,1,0]
	ds_read_b128 v[84:87], v93 offset:10240
	ds_read_b128 v[132:135], v93 offset:10256
	ds_read_b128 v[136:139], v93 offset:12288
	ds_read_b128 v[140:143], v93 offset:12304
	v_pk_add_f32 v[24:25], v[24:25], v[32:33]
	v_mov_b32_e32 v32, v106
	v_mov_b32_e32 v33, v30
	v_mov_b32_e32 v28, v102
	v_mov_b32_e32 v29, v26
	v_pk_mul_f32 v[32:33], v[32:33], v[78:79] op_sel_hi:[1,0]
	v_mov_b32_e32 v30, v107
	v_pk_fma_f32 v[28:29], v[28:29], v[74:75], v[32:33] op_sel_hi:[1,0,1]
	v_mov_b32_e32 v26, v103
	v_pk_add_f32 v[24:25], v[28:29], v[24:25]
	v_pk_mul_f32 v[28:29], v[30:31], v[78:79] op_sel:[0,1]
	v_mov_b32_e32 v32, v59
	v_pk_fma_f32 v[26:27], v[26:27], v[74:75], v[28:29] op_sel:[0,1,0]
	v_mov_b32_e32 v28, v112
	s_waitcnt lgkmcnt(2)
	v_mov_b32_e32 v29, v132
	v_pk_add_f32 v[24:25], v[26:27], v[24:25]
	v_mov_b32_e32 v26, v108
	v_mov_b32_e32 v27, v84
	v_pk_mul_f32 v[28:29], v[28:29], v[76:77] op_sel_hi:[1,0]
	v_mov_b32_e32 v132, v113
	v_pk_fma_f32 v[26:27], v[26:27], v[72:73], v[28:29] op_sel_hi:[1,0,1]
	v_mov_b32_e32 v84, v109
	v_pk_add_f32 v[24:25], v[26:27], v[24:25]
	v_pk_mul_f32 v[26:27], v[132:133], v[76:77] op_sel:[0,1]
	v_mov_b32_e32 v28, v114
	v_pk_fma_f32 v[26:27], v[84:85], v[72:73], v[26:27] op_sel:[0,1,0]
	v_mov_b32_e32 v29, v134
	v_pk_add_f32 v[24:25], v[26:27], v[24:25]
	v_mov_b32_e32 v26, v110
	v_mov_b32_e32 v27, v86
	v_pk_mul_f32 v[28:29], v[28:29], v[70:71] op_sel_hi:[1,0]
	v_mov_b32_e32 v134, v115
	v_pk_fma_f32 v[26:27], v[26:27], v[66:67], v[28:29] op_sel_hi:[1,0,1]
	v_mov_b32_e32 v86, v111
	v_pk_add_f32 v[24:25], v[26:27], v[24:25]
	v_pk_mul_f32 v[26:27], v[134:135], v[70:71] op_sel:[0,1]
	v_mov_b32_e32 v28, v120
	v_pk_fma_f32 v[26:27], v[86:87], v[66:67], v[26:27] op_sel:[0,1,0]
	s_waitcnt lgkmcnt(0)
	v_mov_b32_e32 v29, v140
	v_pk_add_f32 v[24:25], v[26:27], v[24:25]
	v_mov_b32_e32 v26, v116
	v_mov_b32_e32 v27, v136
	v_pk_mul_f32 v[28:29], v[28:29], v[68:69] op_sel_hi:[1,0]
	v_mov_b32_e32 v140, v121
	v_pk_fma_f32 v[26:27], v[26:27], v[64:65], v[28:29] op_sel_hi:[1,0,1]
	v_mov_b32_e32 v136, v117
	v_pk_add_f32 v[24:25], v[26:27], v[24:25]
	v_pk_mul_f32 v[26:27], v[140:141], v[68:69] op_sel:[0,1]
	v_mov_b32_e32 v28, v122
	v_pk_fma_f32 v[26:27], v[136:137], v[64:65], v[26:27] op_sel:[0,1,0]
	v_mov_b32_e32 v29, v142
	v_pk_add_f32 v[24:25], v[26:27], v[24:25]
	v_mov_b32_e32 v26, v118
	v_mov_b32_e32 v27, v138
	v_pk_mul_f32 v[28:29], v[28:29], v[60:61] op_sel_hi:[1,0]
	v_mov_b32_e32 v138, v123
	v_pk_fma_f32 v[26:27], v[26:27], v[58:59], v[28:29] op_sel_hi:[1,0,1]
	v_mov_b32_e32 v142, v119
	v_pk_add_f32 v[28:29], v[26:27], v[24:25]
	v_mov_b32_e32 v24, v61
	v_mov_b32_e32 v25, v59
	v_pk_mul_f32 v[30:31], v[138:139], v[24:25]
	v_mov_b32_e32 v33, v61
	ds_read_b128 v[24:27], v93 offset:14336
	v_pk_fma_f32 v[30:31], v[142:143], v[32:33], v[30:31]
	v_mov_b32_e32 v84, v128
	v_pk_add_f32 v[32:33], v[30:31], v[28:29]
	ds_read_b128 v[28:31], v93 offset:14352
	s_waitcnt lgkmcnt(1)
	v_mov_b32_e32 v85, v24
	v_pk_mul_f32 v[84:85], v[84:85], v[62:63] op_sel:[0,1] op_sel_hi:[1,0]
	v_mov_b32_e32 v86, v124
	v_mov_b32_e32 v24, v129
	s_waitcnt lgkmcnt(0)
	v_mov_b32_e32 v87, v28
	v_pk_fma_f32 v[84:85], v[86:87], v[62:63], v[84:85]
	v_pk_mul_f32 v[24:25], v[24:25], v[18:19] op_sel:[0,1] op_sel_hi:[1,0]
	v_mov_b32_e32 v28, v125
	v_pk_add_f32 v[32:33], v[84:85], v[32:33]
	v_pk_fma_f32 v[24:25], v[28:29], v[18:19], v[24:25]
	v_mov_b32_e32 v28, v130
	v_mov_b32_e32 v29, v26
	v_pk_add_f32 v[24:25], v[24:25], v[32:33]
	v_pk_mul_f32 v[28:29], v[28:29], v[22:23] op_sel:[0,1] op_sel_hi:[1,0]
	v_mov_b32_e32 v32, v126
	v_mov_b32_e32 v33, v30
	v_mov_b32_e32 v26, v131
	v_pk_fma_f32 v[28:29], v[32:33], v[22:23], v[28:29]
	v_pk_mul_f32 v[26:27], v[26:27], v[20:21] op_sel:[0,1] op_sel_hi:[1,0]
	v_mov_b32_e32 v30, v127
	v_pk_add_f32 v[24:25], v[28:29], v[24:25]
	v_pk_fma_f32 v[26:27], v[30:31], v[20:21], v[26:27]
	s_nop 0
	v_pk_add_f32 v[24:25], v[26:27], v[24:25]
	ds_bpermute_b32 v26, v1, v24
	ds_bpermute_b32 v27, v1, v25
	s_waitcnt lgkmcnt(0)
	v_pk_add_f32 v[24:25], v[24:25], v[26:27]
	ds_bpermute_b32 v26, v88, v24
	ds_bpermute_b32 v27, v88, v25
	s_waitcnt lgkmcnt(0)
	v_pk_add_f32 v[24:25], v[24:25], v[26:27]
	ds_bpermute_b32 v26, v89, v24
	ds_bpermute_b32 v27, v89, v25
	s_waitcnt lgkmcnt(0)
	v_pk_add_f32 v[24:25], v[24:25], v[26:27]
	ds_bpermute_b32 v26, v90, v24
	ds_bpermute_b32 v27, v90, v25
	s_waitcnt lgkmcnt(0)
	v_pk_add_f32 v[24:25], v[24:25], v[26:27]
	ds_read_b128 v[26:29], v93 offset:16400
	ds_read_b128 v[30:33], v93 offset:16384
	ds_bpermute_b32 v84, v91, v24
	ds_bpermute_b32 v85, v91, v25
	s_waitcnt lgkmcnt(3)
	v_mul_f32_e32 v26, v82, v26
	s_waitcnt lgkmcnt(2)
	v_fmac_f32_e32 v26, v80, v30
	v_mul_f32_e32 v27, v83, v27
	s_waitcnt lgkmcnt(0)
	v_pk_add_f32 v[24:25], v[24:25], v[84:85]
	v_add_f32_e32 v26, 0, v26
	v_fmac_f32_e32 v27, v81, v31
	ds_read_b128 v[84:87], v93 offset:18432
	ds_read_b128 v[100:103], v93 offset:18448
	v_add_f32_e32 v26, v27, v26
	v_mul_f32_e32 v27, v78, v28
	v_fmac_f32_e32 v27, v74, v32
	v_add_f32_e32 v26, v27, v26
	v_mul_f32_e32 v27, v79, v29
	v_fmac_f32_e32 v27, v75, v33
	v_add_f32_e32 v26, v27, v26
	s_waitcnt lgkmcnt(0)
	v_mul_f32_e32 v27, v76, v100
	v_fmac_f32_e32 v27, v72, v84
	v_add_f32_e32 v26, v27, v26
	v_mul_f32_e32 v27, v77, v101
	v_fmac_f32_e32 v27, v73, v85
	v_add_f32_e32 v38, v27, v26
	ds_read_b128 v[26:29], v93 offset:20480
	ds_read_b128 v[30:33], v93 offset:20496
	v_mul_f32_e32 v84, v70, v102
	v_fmac_f32_e32 v84, v66, v86
	v_add_f32_e32 v38, v84, v38
	v_mul_f32_e32 v84, v71, v103
	v_fmac_f32_e32 v84, v67, v87
	s_waitcnt lgkmcnt(0)
	v_mul_f32_e32 v30, v68, v30
	v_add_f32_e32 v38, v84, v38
	v_fmac_f32_e32 v30, v64, v26
	v_add_f32_e32 v26, v30, v38
	v_mul_f32_e32 v30, v69, v31
	ds_read_b128 v[84:87], v93 offset:22528
	ds_read_b128 v[100:103], v93 offset:22544
	v_fmac_f32_e32 v30, v65, v27
	v_mul_f32_e32 v27, v60, v32
	v_add_f32_e32 v26, v30, v26
	v_fmac_f32_e32 v27, v58, v28
	v_add_f32_e32 v26, v27, v26
	v_mul_f32_e32 v27, v61, v33
	v_fmac_f32_e32 v27, v59, v29
	v_add_f32_e32 v26, v27, v26
	s_waitcnt lgkmcnt(0)
	v_mul_f32_e32 v27, v63, v100
	v_fmac_f32_e32 v27, v62, v84
	v_add_f32_e32 v26, v27, v26
	v_mul_f32_e32 v27, v19, v101
	v_fmac_f32_e32 v27, v18, v85
	v_add_f32_e32 v26, v27, v26
	v_mul_f32_e32 v27, v23, v102
	v_fmac_f32_e32 v27, v22, v86
	v_add_f32_e32 v26, v27, v26
	v_mul_f32_e32 v27, v21, v103
	v_fmac_f32_e32 v27, v20, v87
	ds_read_b128 v[28:31], v93 offset:24576
	ds_read_b128 v[84:87], v93 offset:24592
	ds_read_b128 v[100:103], v93 offset:26624
	ds_read_b128 v[104:107], v93 offset:26640
	v_add_f32_e32 v32, v27, v26
	ds_bpermute_b32 v33, v1, v32
	ds_bpermute_b32 v26, v92, v24
	s_waitcnt lgkmcnt(4)
	v_mul_f32_e32 v38, v82, v84
	v_fmac_f32_e32 v38, v80, v28
	v_add_f32_e32 v28, 0, v38
	v_mul_f32_e32 v38, v83, v85
	v_fmac_f32_e32 v38, v81, v29
	v_mul_f32_e32 v29, v78, v86
	v_add_f32_e32 v28, v38, v28
	v_fmac_f32_e32 v29, v74, v30
	v_add_f32_e32 v28, v29, v28
	v_mul_f32_e32 v29, v79, v87
	v_fmac_f32_e32 v29, v75, v31
	v_add_f32_e32 v28, v29, v28
	s_waitcnt lgkmcnt(2)
	v_mul_f32_e32 v29, v76, v104
	v_fmac_f32_e32 v29, v72, v100
	v_add_f32_e32 v28, v29, v28
	v_mul_f32_e32 v29, v77, v105
	v_fmac_f32_e32 v29, v73, v101
	v_add_f32_e32 v38, v29, v28
	ds_read_b128 v[28:31], v93 offset:28672
	ds_read_b128 v[84:87], v93 offset:28688
	v_mul_f32_e32 v100, v70, v106
	v_fmac_f32_e32 v100, v66, v102
	v_add_f32_e32 v38, v100, v38
	v_mul_f32_e32 v100, v71, v107
	v_fmac_f32_e32 v100, v67, v103
	s_waitcnt lgkmcnt(0)
	v_mul_f32_e32 v84, v68, v84
	v_add_f32_e32 v38, v100, v38
	v_fmac_f32_e32 v84, v64, v28
	v_add_f32_e32 v28, v84, v38
	v_mul_f32_e32 v38, v69, v85
	ds_read_b128 v[100:103], v93 offset:30720
	ds_read_b128 v[104:107], v93 offset:30736
	v_fmac_f32_e32 v38, v65, v29
	v_mul_f32_e32 v29, v60, v86
	v_add_f32_e32 v28, v38, v28
	v_fmac_f32_e32 v29, v58, v30
	v_add_f32_e32 v28, v29, v28
	v_mul_f32_e32 v29, v61, v87
	v_fmac_f32_e32 v29, v59, v31
	v_add_f32_e32 v28, v29, v28
	s_waitcnt lgkmcnt(0)
	v_mul_f32_e32 v29, v63, v104
	v_fmac_f32_e32 v29, v62, v100
	v_add_f32_e32 v28, v29, v28
	v_mul_f32_e32 v29, v19, v105
	v_fmac_f32_e32 v29, v18, v101
	v_add_f32_e32 v28, v29, v28
	v_mul_f32_e32 v29, v23, v106
	v_fmac_f32_e32 v29, v22, v102
	v_add_f32_e32 v38, v29, v28
	ds_read_b128 v[28:31], v93 offset:32768
	ds_read_b128 v[84:87], v93 offset:32784
	v_mul_f32_e32 v100, v21, v107
	v_fmac_f32_e32 v100, v20, v103
	v_add_f32_e32 v38, v100, v38
	ds_read_b128 v[100:103], v93 offset:34816
	ds_read_b128 v[104:107], v93 offset:34832
	s_waitcnt lgkmcnt(2)
	v_mul_f32_e32 v84, v82, v84
	v_fmac_f32_e32 v84, v80, v28
	v_add_f32_e32 v28, 0, v84
	v_mul_f32_e32 v84, v83, v85
	v_fmac_f32_e32 v84, v81, v29
	v_mul_f32_e32 v29, v78, v86
	v_add_f32_e32 v28, v84, v28
	v_fmac_f32_e32 v29, v74, v30
	v_add_f32_e32 v28, v29, v28
	v_mul_f32_e32 v29, v79, v87
	v_fmac_f32_e32 v29, v75, v31
	v_add_f32_e32 v28, v29, v28
	s_waitcnt lgkmcnt(0)
	v_mul_f32_e32 v29, v76, v104
	v_fmac_f32_e32 v29, v72, v100
	v_add_f32_e32 v28, v29, v28
	v_mul_f32_e32 v29, v77, v105
	v_fmac_f32_e32 v29, v73, v101
	v_add_f32_e32 v100, v29, v28
	ds_read_b128 v[28:31], v93 offset:36864
	ds_read_b128 v[84:87], v93 offset:36880
	v_mul_f32_e32 v101, v70, v106
	v_fmac_f32_e32 v101, v66, v102
	v_add_f32_e32 v100, v101, v100
	v_mul_f32_e32 v101, v71, v107
	v_fmac_f32_e32 v101, v67, v103
	s_waitcnt lgkmcnt(0)
	v_mul_f32_e32 v84, v68, v84
	v_add_f32_e32 v100, v101, v100
	v_fmac_f32_e32 v84, v64, v28
	v_add_f32_e32 v28, v84, v100
	v_mul_f32_e32 v84, v69, v85
	ds_read_b128 v[100:103], v93 offset:38912
	ds_read_b128 v[104:107], v93 offset:38928
	v_fmac_f32_e32 v84, v65, v29
	v_mul_f32_e32 v29, v60, v86
	v_add_f32_e32 v28, v84, v28
	v_fmac_f32_e32 v29, v58, v30
	v_add_f32_e32 v28, v29, v28
	v_mul_f32_e32 v29, v61, v87
	v_fmac_f32_e32 v29, v59, v31
	v_add_f32_e32 v28, v29, v28
	s_waitcnt lgkmcnt(0)
	v_mul_f32_e32 v29, v63, v104
	v_fmac_f32_e32 v29, v62, v100
	v_add_f32_e32 v28, v29, v28
	v_mul_f32_e32 v29, v19, v105
	v_fmac_f32_e32 v29, v18, v101
	v_add_f32_e32 v28, v29, v28
	v_mul_f32_e32 v29, v23, v106
	v_fmac_f32_e32 v29, v22, v102
	v_add_f32_e32 v28, v29, v28
	v_mul_f32_e32 v29, v21, v107
	v_fmac_f32_e32 v29, v20, v103
	v_add_f32_e32 v32, v32, v33
	v_add_f32_e32 v28, v29, v28
	ds_bpermute_b32 v33, v88, v32
	ds_bpermute_b32 v108, v1, v38
	ds_bpermute_b32 v29, v1, v28
	ds_bpermute_b32 v27, v92, v25
	s_waitcnt lgkmcnt(3)
	v_add_f32_e32 v30, v32, v33
	s_waitcnt lgkmcnt(2)
	v_add_f32_e32 v32, v38, v108
	s_waitcnt lgkmcnt(1)
	v_add_f32_e32 v28, v28, v29
	ds_bpermute_b32 v31, v89, v30
	ds_bpermute_b32 v33, v88, v32
	ds_bpermute_b32 v29, v88, v28
	s_waitcnt lgkmcnt(2)
	v_add_f32_e32 v30, v30, v31
	s_waitcnt lgkmcnt(1)
	v_add_f32_e32 v32, v32, v33
	s_waitcnt lgkmcnt(0)
	v_add_f32_e32 v28, v28, v29
	ds_bpermute_b32 v31, v90, v30
	ds_bpermute_b32 v33, v89, v32
	ds_bpermute_b32 v29, v89, v28
	s_waitcnt lgkmcnt(2)
	v_add_f32_e32 v30, v30, v31
	s_waitcnt lgkmcnt(1)
	v_add_f32_e32 v32, v32, v33
	s_waitcnt lgkmcnt(0)
	v_add_f32_e32 v38, v28, v29
	ds_bpermute_b32 v31, v91, v30
	ds_bpermute_b32 v33, v90, v32
	ds_bpermute_b32 v84, v90, v38
	s_waitcnt lgkmcnt(2)
	v_add_f32_e32 v28, v30, v31
	s_waitcnt lgkmcnt(1)
	v_add_f32_e32 v30, v32, v33
	s_waitcnt lgkmcnt(0)
	v_add_f32_e32 v32, v38, v84
	ds_read_b128 v[84:87], v93 offset:40960
	ds_read_b128 v[100:103], v93 offset:40976
	ds_read_b128 v[104:107], v93 offset:43008
	ds_read_b128 v[108:111], v93 offset:43024
	ds_bpermute_b32 v31, v91, v30
	ds_bpermute_b32 v33, v91, v32
	ds_bpermute_b32 v29, v92, v28
	s_waitcnt lgkmcnt(5)
	v_mul_f32_e32 v38, v82, v100
	v_fmac_f32_e32 v38, v80, v84
	v_mul_f32_e32 v84, v83, v101
	v_add_f32_e32 v38, 0, v38
	v_fmac_f32_e32 v84, v81, v85
	v_add_f32_e32 v38, v84, v38
	v_mul_f32_e32 v84, v78, v102
	v_fmac_f32_e32 v84, v74, v86
	v_add_f32_e32 v38, v84, v38
	v_mul_f32_e32 v84, v79, v103
	v_fmac_f32_e32 v84, v75, v87
	v_add_f32_e32 v38, v84, v38
	s_waitcnt lgkmcnt(3)
	v_mul_f32_e32 v84, v76, v108
	v_fmac_f32_e32 v84, v72, v104
	v_add_f32_e32 v38, v84, v38
	v_mul_f32_e32 v84, v77, v109
	v_fmac_f32_e32 v84, v73, v105
	v_add_f32_e32 v38, v84, v38
	ds_read_b128 v[84:87], v93 offset:45056
	ds_read_b128 v[100:103], v93 offset:45072
	v_mul_f32_e32 v104, v70, v110
	v_fmac_f32_e32 v104, v66, v106
	v_add_f32_e32 v38, v104, v38
	v_mul_f32_e32 v104, v71, v111
	v_fmac_f32_e32 v104, v67, v107
	s_waitcnt lgkmcnt(0)
	v_mul_f32_e32 v100, v68, v100
	v_add_f32_e32 v38, v104, v38
	v_fmac_f32_e32 v100, v64, v84
	v_mul_f32_e32 v84, v69, v101
	v_add_f32_e32 v38, v100, v38
	v_fmac_f32_e32 v84, v65, v85
	ds_read_b128 v[104:107], v93 offset:47104
	ds_read_b128 v[108:111], v93 offset:47120
	v_add_f32_e32 v38, v84, v38
	v_mul_f32_e32 v84, v60, v102
	v_fmac_f32_e32 v84, v58, v86
	v_add_f32_e32 v38, v84, v38
	v_mul_f32_e32 v84, v61, v103
	v_fmac_f32_e32 v84, v59, v87
	v_add_f32_e32 v38, v84, v38
	s_waitcnt lgkmcnt(0)
	v_mul_f32_e32 v84, v63, v108
	v_fmac_f32_e32 v84, v62, v104
	v_add_f32_e32 v38, v84, v38
	v_mul_f32_e32 v84, v19, v109
	v_fmac_f32_e32 v84, v18, v105
	v_add_f32_e32 v38, v84, v38
	v_mul_f32_e32 v84, v23, v110
	v_fmac_f32_e32 v84, v22, v106
	v_add_f32_e32 v38, v84, v38
	ds_read_b128 v[84:87], v93 offset:49152
	ds_read_b128 v[100:103], v93 offset:49168
	v_mul_f32_e32 v104, v21, v111
	v_fmac_f32_e32 v104, v20, v107
	v_add_f32_e32 v38, v104, v38
	ds_read_b128 v[104:107], v93 offset:51200
	ds_read_b128 v[108:111], v93 offset:51216
	s_waitcnt lgkmcnt(2)
	v_mul_f32_e32 v100, v82, v100
	v_fmac_f32_e32 v100, v80, v84
	v_add_f32_e32 v84, 0, v100
	v_mul_f32_e32 v100, v83, v101
	v_fmac_f32_e32 v100, v81, v85
	v_mul_f32_e32 v85, v78, v102
	v_add_f32_e32 v84, v100, v84
	v_fmac_f32_e32 v85, v74, v86
	v_add_f32_e32 v84, v85, v84
	v_mul_f32_e32 v85, v79, v103
	v_fmac_f32_e32 v85, v75, v87
	v_add_f32_e32 v84, v85, v84
	s_waitcnt lgkmcnt(0)
	v_mul_f32_e32 v85, v76, v108
	v_fmac_f32_e32 v85, v72, v104
	v_add_f32_e32 v84, v85, v84
	v_mul_f32_e32 v85, v77, v109
	v_fmac_f32_e32 v85, v73, v105
	v_add_f32_e32 v104, v85, v84
	ds_read_b128 v[84:87], v93 offset:53248
	ds_read_b128 v[100:103], v93 offset:53264
	v_mul_f32_e32 v105, v70, v110
	v_fmac_f32_e32 v105, v66, v106
	v_add_f32_e32 v104, v105, v104
	v_mul_f32_e32 v105, v71, v111
	v_fmac_f32_e32 v105, v67, v107
	s_waitcnt lgkmcnt(0)
	v_mul_f32_e32 v100, v68, v100
	v_add_f32_e32 v104, v105, v104
	v_fmac_f32_e32 v100, v64, v84
	v_add_f32_e32 v84, v100, v104
	v_mul_f32_e32 v100, v69, v101
	ds_read_b128 v[104:107], v93 offset:55296
	ds_read_b128 v[108:111], v93 offset:55312
	v_fmac_f32_e32 v100, v65, v85
	v_mul_f32_e32 v85, v60, v102
	v_add_f32_e32 v84, v100, v84
	v_fmac_f32_e32 v85, v58, v86
	v_add_f32_e32 v84, v85, v84
	v_mul_f32_e32 v85, v61, v103
	v_fmac_f32_e32 v85, v59, v87
	v_add_f32_e32 v84, v85, v84
	s_waitcnt lgkmcnt(0)
	v_mul_f32_e32 v85, v63, v108
	v_fmac_f32_e32 v85, v62, v104
	v_add_f32_e32 v84, v85, v84
	v_mul_f32_e32 v85, v19, v109
	v_fmac_f32_e32 v85, v18, v105
	v_add_f32_e32 v84, v85, v84
	v_mul_f32_e32 v85, v23, v110
	v_fmac_f32_e32 v85, v22, v106
	v_add_f32_e32 v104, v85, v84
	ds_read_b128 v[84:87], v93 offset:57344
	ds_read_b128 v[100:103], v93 offset:57360
	v_mul_f32_e32 v105, v21, v111
	v_fmac_f32_e32 v105, v20, v107
	v_add_f32_e32 v108, v105, v104
	ds_bpermute_b32 v112, v1, v38
	s_waitcnt lgkmcnt(1)
	v_mul_f32_e32 v82, v82, v100
	v_fmac_f32_e32 v82, v80, v84
	v_add_f32_e32 v80, 0, v82
	v_mul_f32_e32 v82, v83, v101
	v_fmac_f32_e32 v82, v81, v85
	v_add_f32_e32 v84, v82, v80
	ds_read_b128 v[80:83], v93 offset:59392
	ds_read_b128 v[104:107], v93 offset:59408
	v_mul_f32_e32 v78, v78, v102
	v_fmac_f32_e32 v78, v74, v86
	v_add_f32_e32 v74, v78, v84
	v_mul_f32_e32 v78, v79, v103
	v_fmac_f32_e32 v78, v75, v87
	s_waitcnt lgkmcnt(0)
	v_mul_f32_e32 v75, v76, v104
	v_add_f32_e32 v74, v78, v74
	v_fmac_f32_e32 v75, v72, v80
	v_add_f32_e32 v72, v75, v74
	v_mul_f32_e32 v74, v77, v105
	v_fmac_f32_e32 v74, v73, v81
	v_add_f32_e32 v80, v74, v72
	ds_read_b128 v[72:75], v93 offset:61440
	ds_read_b128 v[76:79], v93 offset:61456
	v_mul_f32_e32 v70, v70, v106
	v_fmac_f32_e32 v70, v66, v82
	v_add_f32_e32 v66, v70, v80
	v_mul_f32_e32 v70, v71, v107
	v_fmac_f32_e32 v70, v67, v83
	s_waitcnt lgkmcnt(0)
	v_mul_f32_e32 v67, v68, v76
	v_add_f32_e32 v66, v70, v66
	v_fmac_f32_e32 v67, v64, v72
	v_add_f32_e32 v64, v67, v66
	v_mul_f32_e32 v66, v69, v77
	v_fmac_f32_e32 v66, v65, v73
	v_add_f32_e32 v72, v66, v64
	ds_read_b128 v[64:67], v93 offset:63488
	ds_read_b128 v[68:71], v93 offset:63504
	v_mul_f32_e32 v60, v60, v78
	v_fmac_f32_e32 v60, v58, v74
	v_add_f32_e32 v58, v60, v72
	v_mul_f32_e32 v60, v61, v79
	v_fmac_f32_e32 v60, v59, v75
	s_waitcnt lgkmcnt(0)
	v_mul_f32_e32 v59, v63, v68
	v_add_f32_e32 v58, v60, v58
	v_fmac_f32_e32 v59, v62, v64
	v_mul_f32_e32 v19, v19, v69
	v_add_f32_e32 v58, v59, v58
	v_fmac_f32_e32 v19, v18, v65
	v_add_f32_e32 v18, v19, v58
	v_mul_f32_e32 v19, v23, v70
	v_fmac_f32_e32 v19, v22, v66
	v_add_f32_e32 v18, v19, v18
	v_mul_f32_e32 v19, v21, v71
	v_fmac_f32_e32 v19, v20, v67
	v_add_f32_e32 v18, v19, v18
	ds_bpermute_b32 v109, v1, v108
	ds_bpermute_b32 v19, v1, v18
	v_add_f32_e32 v20, v38, v112
	ds_bpermute_b32 v21, v88, v20
	v_add_f32_e32 v30, v30, v31
	s_waitcnt lgkmcnt(2)
	v_add_f32_e32 v22, v108, v109
	s_waitcnt lgkmcnt(1)
	v_add_f32_e32 v18, v18, v19
	ds_bpermute_b32 v23, v88, v22
	ds_bpermute_b32 v19, v88, v18
	s_waitcnt lgkmcnt(2)
	v_add_f32_e32 v20, v20, v21
	ds_bpermute_b32 v21, v89, v20
	v_add_f32_e32 v32, v32, v33
	s_waitcnt lgkmcnt(2)
	v_add_f32_e32 v22, v22, v23
	s_waitcnt lgkmcnt(1)
	v_add_f32_e32 v18, v18, v19
	ds_bpermute_b32 v23, v89, v22
	ds_bpermute_b32 v19, v89, v18
	s_waitcnt lgkmcnt(2)
	v_add_f32_e32 v20, v20, v21
	ds_bpermute_b32 v21, v90, v20
	ds_bpermute_b32 v31, v92, v30
	s_waitcnt lgkmcnt(3)
	v_add_f32_e32 v22, v22, v23
	s_waitcnt lgkmcnt(2)
	v_add_f32_e32 v18, v18, v19
	ds_bpermute_b32 v23, v90, v22
	ds_bpermute_b32 v19, v90, v18
	s_waitcnt lgkmcnt(3)
	v_add_f32_e32 v20, v20, v21
	ds_bpermute_b32 v21, v91, v20
	ds_bpermute_b32 v33, v92, v32
	s_waitcnt lgkmcnt(3)
	v_add_f32_e32 v22, v22, v23
	s_waitcnt lgkmcnt(2)
	v_add_f32_e32 v38, v18, v19
	ds_bpermute_b32 v23, v91, v22
	ds_bpermute_b32 v58, v91, v38
	s_waitcnt lgkmcnt(3)
	v_add_f32_e32 v18, v20, v21
	ds_bpermute_b32 v19, v92, v18
	s_waitcnt lgkmcnt(2)
	v_add_f32_e32 v20, v22, v23
	s_waitcnt lgkmcnt(1)
	v_add_f32_e32 v22, v38, v58
	ds_bpermute_b32 v21, v92, v20
	ds_bpermute_b32 v23, v92, v22
	s_and_saveexec_b64 s[42:43], s[4:5]
	s_cbranch_execz .LBB0_1885
	s_waitcnt lgkmcnt(1)
	v_add_f32_e32 v20, v20, v21
	v_add_f32_e32 v21, v18, v19
	v_pk_add_f32 v[18:19], v[24:25], v[26:27]
	v_add_f32_e32 v28, v28, v29
	v_cmp_gt_f32_e32 vcc, v19, v18
	s_waitcnt lgkmcnt(0)
	v_add_f32_e32 v58, v22, v23
	v_add_f32_e32 v23, v30, v31
	v_cndmask_b32_e32 v24, v18, v19, vcc
	v_cmp_gt_f32_e64 s[0:1], v28, v24
	v_add_f32_e32 v22, v32, v33
	v_cndmask_b32_e64 v25, 0, 1, vcc
	v_cndmask_b32_e64 v24, v24, v28, s[0:1]
	v_cmp_gt_f32_e64 s[8:9], v23, v24
	v_cndmask_b32_e64 v25, v25, 2, s[0:1]
	v_cmp_nlt_f32_e64 s[18:19], s48, v18
	v_cndmask_b32_e64 v24, v24, v23, s[8:9]
	v_cmp_gt_f32_e64 s[10:11], v22, v24
	v_cndmask_b32_e64 v25, v25, 3, s[8:9]
	s_nop 0
	v_cndmask_b32_e64 v24, v24, v22, s[10:11]
	v_cmp_gt_f32_e64 s[12:13], v21, v24
	v_cndmask_b32_e64 v25, v25, 4, s[10:11]
	s_nop 0
	v_cndmask_b32_e64 v24, v24, v21, s[12:13]
	v_cmp_gt_f32_e64 s[14:15], v20, v24
	v_cndmask_b32_e64 v25, v25, 5, s[12:13]
	s_nop 0
	v_cndmask_b32_e64 v24, v24, v20, s[14:15]
	v_cndmask_b32_e64 v25, v25, 6, s[14:15]
	v_cmp_ngt_f32_e32 vcc, v58, v24
	s_and_b64 s[20:21], s[14:15], vcc
	s_nop 0
	v_cndmask_b32_e32 v38, 7, v25, vcc
	v_cmp_eq_u32_e64 s[16:17], 0, v38
	s_or_b64 s[16:17], s[16:17], s[18:19]
	v_cmp_ne_u32_e64 s[14:15], 1, v38
	v_cndmask_b32_e64 v18, v18, v97, s[16:17]
	v_cmp_gt_f32_e64 s[18:19], v19, v18
	s_and_b64 s[14:15], s[14:15], s[18:19]
	v_cndmask_b32_e64 v18, v18, v19, s[14:15]
	v_cmp_ne_u32_e64 s[12:13], 2, v38
	v_cmp_gt_f32_e64 s[18:19], v28, v18
	s_and_b64 s[12:13], s[12:13], s[18:19]
	v_cndmask_b32_e64 v18, v18, v28, s[12:13]
	v_cmp_ne_u32_e64 s[10:11], 3, v38
	v_cmp_gt_f32_e64 s[18:19], v23, v18
	s_and_b64 s[10:11], s[10:11], s[18:19]
	v_cndmask_b32_e64 v18, v18, v23, s[10:11]
	v_cmp_ne_u32_e64 s[8:9], 4, v38
	v_cmp_gt_f32_e64 s[18:19], v22, v18
	s_and_b64 s[8:9], s[8:9], s[18:19]
	v_cndmask_b32_e64 v18, v18, v22, s[8:9]
	v_cmp_ne_u32_e64 s[0:1], 5, v38
	v_cmp_gt_f32_e64 s[18:19], v21, v18
	s_and_b64 s[0:1], s[0:1], s[18:19]
	v_cndmask_b32_e64 v18, v18, v21, s[0:1]
	v_cmp_ngt_f32_e64 s[18:19], v20, v18
	s_or_b64 s[18:19], s[20:21], s[18:19]
	s_nop 0
	v_cndmask_b32_e64 v18, v20, v18, s[18:19]
	v_cmp_gt_f32_e64 s[20:21], v58, v18
	s_and_b64 s[20:21], vcc, s[20:21]
	s_nop 0
	v_cndmask_b32_e64 v25, v18, v58, s[20:21]
	v_cndmask_b32_e64 v18, 0, -1, s[16:17]
	v_cndmask_b32_e64 v18, v18, 1, s[14:15]
	v_cndmask_b32_e64 v18, v18, 2, s[12:13]
	v_cndmask_b32_e64 v18, v18, 3, s[10:11]
	v_cndmask_b32_e64 v18, v18, 4, s[8:9]
	v_cndmask_b32_e64 v18, v18, 5, s[0:1]
	v_cndmask_b32_e64 v18, 6, v18, s[18:19]
	v_cndmask_b32_e64 v22, v18, 7, s[20:21]
	s_cmp_eq_u32 s98, 0
	s_cbranch_scc1 .Lln3_nopend
	s_waitcnt vmcnt(0)
	global_store_dwordx4 v[210:211], v[204:207], off
	global_store_dwordx2 v[210:211], v[208:209], off offset:16
	v_lshl_add_u32 v214, v204, 14, v206
	v_ashrrev_i32_e32 v215, 31, v214
	v_lshl_add_u64 v[214:215], v[214:215], 2, s[30:31]
	global_store_dword v[214:215], v212, off
	v_lshl_add_u32 v214, v205, 14, v207
	v_ashrrev_i32_e32 v215, 31, v214
	v_lshl_add_u64 v[214:215], v[214:215], 2, s[30:31]
	global_store_dword v[214:215], v212, off
.Lln3_nopend:
	v_lshl_add_u64 v[18:19], v[38:39], 2, s[28:29]
	v_ashrrev_i32_e32 v23, 31, v22
	global_atomic_add v206, v[18:19], v95, off sc0
	v_lshl_add_u64 v[18:19], v[22:23], 2, s[28:29]
	global_atomic_add v207, v[18:19], v95, off sc0
	v_cndmask_b32_e32 v18, v58, v24, vcc
	v_sub_f32_e32 v18, v25, v18
	v_mul_f32_e32 v19, 0x3fb8aa3b, v18
	v_fma_f32 v23, v18, s49, -v19
	v_rndne_f32_e32 v24, v19
	v_fmac_f32_e32 v23, 0x32a5705f, v18
	v_sub_f32_e32 v19, v19, v24
	v_add_f32_e32 v19, v19, v23
	v_exp_f32_e32 v19, v19
	v_cvt_i32_f32_e32 v23, v24
	v_cmp_ngt_f32_e32 vcc, s50, v18
	v_ldexp_f32 v19, v19, v23
	s_nop 0
	v_cndmask_b32_e32 v19, 0, v19, vcc
	v_cmp_nlt_f32_e32 vcc, s51, v18
	s_nop 1
	v_cndmask_b32_e32 v18, v98, v19, vcc
	v_add_f32_e32 v18, 1.0, v18
	v_div_scale_f32 v19, s[0:1], v18, v18, 1.0
	v_rcp_f32_e32 v23, v19
	s_nop 0
	v_fma_f32 v24, -v19, v23, 1.0
	v_fmac_f32_e32 v23, v24, v23
	v_div_scale_f32 v24, vcc, 1.0, v18, 1.0
	v_mul_f32_e32 v25, v24, v23
	v_fma_f32 v26, -v19, v25, v24
	v_fmac_f32_e32 v25, v26, v23
	v_fma_f32 v19, -v19, v25, v24
	v_lshl_add_u64 v[26:27], s[58:59], 0, v[54:55]
	v_div_fmas_f32 v19, v19, v23, v25
	v_add_co_u32_e32 v26, vcc, s60, v26
	v_div_fixup_f32 v24, v19, v18, 1.0
	v_mov_b32_e32 v204, v38
	v_mov_b32_e32 v205, v22
	v_addc_co_u32_e32 v27, vcc, 0, v27, vcc
	v_sub_f32_e32 v25, 1.0, v24
	v_mov_b32_e32 v208, v24
	v_mov_b32_e32 v209, v25
	v_mov_b32_e32 v210, v26
	v_mov_b32_e32 v211, v27
	v_mov_b32_e32 v212, v34
	s_mov_b32 s98, 1
	s_branch .LBB0_1885
.LBB0_1888:
	s_or_b64 exec, exec, s[24:25]
	s_cmp_eq_u32 s98, 0
	s_cbranch_scc1 .Lln3_nopend2
	s_mov_b64 s[0:1], exec
	s_mov_b64 exec, 1
	s_waitcnt vmcnt(0)
	global_store_dwordx4 v[210:211], v[204:207], off
	global_store_dwordx2 v[210:211], v[208:209], off offset:16
	v_lshl_add_u32 v214, v204, 14, v206
	v_ashrrev_i32_e32 v215, 31, v214
	v_lshl_add_u64 v[214:215], v[214:215], 2, s[30:31]
	global_store_dword v[214:215], v212, off
	v_lshl_add_u32 v214, v205, 14, v207
	v_ashrrev_i32_e32 v215, 31, v214
	v_lshl_add_u64 v[214:215], v[214:215], 2, s[30:31]
	global_store_dword v[214:215], v212, off
	s_mov_b64 exec, s[0:1]
	s_mov_b32 s98, 0
.Lln3_nopend2:
.LBB0_1889:
	s_cmp_gt_i32 s77, 17
	s_cselect_b64 s[0:1], -1, 0
	s_and_b64 s[4:5], s[22:23], s[0:1]
	s_andn2_b64 vcc, exec, s[4:5]
	s_cbranch_vccnz .LBB0_1943
	s_waitcnt vmcnt(0)
	s_waitcnt vmcnt(0) lgkmcnt(0)
	s_barrier
	s_mov_b64 s[4:5], exec
	v_readlane_b32 s6, v239, 16
	v_readlane_b32 s7, v239, 17
	s_and_b64 s[6:7], s[4:5], s[6:7]
	s_mov_b64 exec, s[6:7]
	s_cbranch_execz .LBB0_1942
	s_add_i32 s3, 0, 0x26020
	v_mov_b32_e32 v1, s3
	s_waitcnt vmcnt(0) expcnt(0) lgkmcnt(0)
	ds_read_b32 v3, v1
	s_add_i32 s3, 0, 0x26024
	v_mov_b32_e32 v1, s3
	ds_read_b32 v1, v1
	s_waitcnt lgkmcnt(1)
	v_cmp_ne_u32_e32 vcc, 0, v3
	s_cbranch_vccnz .LBB0_1906
	v_readlane_b32 s6, v239, 34
	v_readlane_b32 s7, v239, 35
	s_load_dwordx2 s[10:11], s[6:7], 0x4
	s_add_u32 s6, s58, 0x1000
	s_addc_u32 s7, s59, 0
	s_add_u32 s8, s58, 0x1100
	s_addc_u32 s9, s59, 0
	s_waitcnt lgkmcnt(0)
	s_mul_i32 s3, s10, s2
	s_add_u32 s10, s58, 0x1200
	s_mul_i32 s3, s3, s11
	s_addc_u32 s11, s59, 0
	s_add_u32 s12, s58, 0x1300
	s_addc_u32 s13, s59, 0
	s_mov_b32 s20, 1
	v_mov_b32_e32 v17, 0
	s_branch .LBB0_1894
